# best version with x-stream loads using nt sc1 cache policy (sc0 dropped)
# speedup vs baseline: 1.0083x; 1.0083x over previous
.LBB1_142:
	s_andn2_b64 vcc, exec, s[4:5]
	s_cbranch_vccnz .LBB1_182
	s_lshl_b32 s12, s23, 3
	s_add_i32 s13, s98, s12
	s_lshl_b32 s3, s13, 10
	s_mov_b32 s7, 0x20000
	s_brev_b32 s6, 16
	s_waitcnt lgkmcnt(0)
	s_and_b32 s5, s17, 0xffff
	s_add_i32 s3, s3, 0x2000000
	s_mov_b32 s8, s16
	s_mov_b32 s9, s5
	s_mov_b32 s10, s6
	s_mov_b32 s11, s7
	s_or_b32 s4, s3, 0x400
	buffer_load_dwordx4 v[126:129], v162, s[8:11], s3 offen nt sc1
	buffer_load_dwordx4 v[122:125], v162, s[8:11], s4 offen nt sc1
	s_or_b32 s4, s3, 0x800
	s_or_b32 s22, s3, 0xc00
	buffer_load_dwordx4 v[118:121], v162, s[8:11], s4 offen nt sc1
	buffer_load_dwordx4 v[114:117], v162, s[8:11], s22 offen nt sc1
	s_or_b32 s4, s3, 0x1000
	s_or_b32 s22, s3, 0x1400
	buffer_load_dwordx4 v[110:113], v162, s[8:11], s4 offen nt sc1
	buffer_load_dwordx4 v[106:109], v162, s[8:11], s22 offen nt sc1
	s_or_b32 s4, s3, 0x1800
	s_or_b32 s22, s3, 0x1c00
	buffer_load_dwordx4 v[102:105], v162, s[8:11], s4 offen nt sc1
	buffer_load_dwordx4 v[94:97], v162, s[8:11], s22 offen nt sc1
	s_or_b32 s4, s3, 0x4000
	s_or_b32 s22, s3, 0x4400
	buffer_load_dwordx4 v[98:101], v162, s[8:11], s4 offen nt sc1
	buffer_load_dwordx4 v[90:93], v162, s[8:11], s22 offen nt sc1
	s_or_b32 s4, s3, 0x4800
	s_or_b32 s22, s3, 0x4c00
	buffer_load_dwordx4 v[86:89], v162, s[8:11], s4 offen nt sc1
	buffer_load_dwordx4 v[82:85], v162, s[8:11], s22 offen nt sc1
	s_or_b32 s4, s3, 0x5000
	s_or_b32 s22, s3, 0x5400
	buffer_load_dwordx4 v[78:81], v162, s[8:11], s4 offen nt sc1
	buffer_load_dwordx4 v[74:77], v162, s[8:11], s22 offen nt sc1
	s_or_b32 s4, s3, 0x5800
	s_or_b32 s22, s3, 0x5c00
	buffer_load_dwordx4 v[66:69], v162, s[8:11], s4 offen nt sc1
	buffer_load_dwordx4 v[58:61], v162, s[8:11], s22 offen nt sc1
	s_or_b32 s4, s3, 0x8000
	s_or_b32 s22, s3, 0x8400
	buffer_load_dwordx4 v[70:73], v162, s[8:11], s4 offen nt sc1
	buffer_load_dwordx4 v[62:65], v162, s[8:11], s22 offen nt sc1
	s_or_b32 s4, s3, 0x8800
	s_or_b32 s22, s3, 0x8c00
	buffer_load_dwordx4 v[54:57], v162, s[8:11], s4 offen nt sc1
	buffer_load_dwordx4 v[50:53], v162, s[8:11], s22 offen nt sc1
	s_or_b32 s4, s3, 0x9000
	s_or_b32 s22, s3, 0x9400
	buffer_load_dwordx4 v[46:49], v162, s[8:11], s4 offen nt sc1
	buffer_load_dwordx4 v[42:45], v162, s[8:11], s22 offen nt sc1
	s_or_b32 s4, s3, 0x9800
	s_or_b32 s22, s3, 0x9c00
	buffer_load_dwordx4 v[34:37], v162, s[8:11], s4 offen nt sc1
	buffer_load_dwordx4 v[26:29], v162, s[8:11], s22 offen nt sc1
	s_or_b32 s4, s3, 0xc000
	s_or_b32 s22, s3, 0xc400
	buffer_load_dwordx4 v[38:41], v162, s[8:11], s4 offen nt sc1
	buffer_load_dwordx4 v[30:33], v162, s[8:11], s22 offen nt sc1
	s_or_b32 s4, s3, 0xc800
	s_or_b32 s22, s3, 0xcc00
	buffer_load_dwordx4 v[22:25], v162, s[8:11], s4 offen nt sc1
	buffer_load_dwordx4 v[18:21], v162, s[8:11], s22 offen nt sc1
	s_or_b32 s4, s3, 0xd000
	s_or_b32 s22, s3, 0xd400
	buffer_load_dwordx4 v[14:17], v162, s[8:11], s4 offen nt sc1
	buffer_load_dwordx4 v[10:13], v162, s[8:11], s22 offen nt sc1
	s_or_b32 s4, s3, 0xd800
	s_or_b32 s3, s3, 0xdc00
	buffer_load_dwordx4 v[6:9], v162, s[8:11], s4 offen nt sc1
	buffer_load_dwordx4 v[2:5], v162, s[8:11], s3 offen nt sc1
	s_mul_i32 s3, s23, 0x1080
	v_lshl_add_u32 v1, v164, 3, s3
	s_or_b32 s11, s98, s12
	s_lshl_b32 s38, s2, 17
	s_mov_b32 s4, s16
	v_mov_b32_e32 v163, 0
	s_lshl_b32 s10, s23, 13
	s_or_b32 s22, s11, 16
	s_or_b32 s23, s11, 32
	s_or_b32 s24, s11, 48
	s_or_b32 s25, s11, 64
	s_or_b32 s26, s11, 0x50
	s_add_i32 s27, s98, 0x8010
	s_or_b32 s28, s11, 0x60
	s_add_i32 s29, s98, 0x8020
	s_or_b32 s30, s11, 0x70
	s_add_i32 s31, s98, 0x8030
	s_add_i32 s34, s38, 0x2010000
	s_add_i32 s35, s38, 0x2014000
	s_add_i32 s36, s38, 0x2018000
	s_add_i32 s37, s38, 0x201c000
	s_add_i32 s38, s38, 0x4000000
	s_mov_b32 s3, 0
	s_mov_b64 s[8:9], -1
	v_mov_b32_e32 v165, 0x22634
	v_add_u32_e32 v166, 0x800, v1
	v_add_u32_e32 v167, 0x2000, v1
	v_add_u32_e32 v168, 0x2800, v1
	v_add_u32_e32 v169, 0x4000, v1
	v_add_u32_e32 v170, 0x4400, v1
	v_add_u32_e32 v171, 0x4800, v1
	v_add_u32_e32 v172, 0x4c00, v1
	v_add_u32_e32 v173, 0x6000, v1
	v_add_u32_e32 v174, 0x6400, v1
	v_add_u32_e32 v175, 0x6800, v1
	v_add_u32_e32 v176, 0x6c00, v1
	v_add_u32_e32 v177, 0x8000, v1
	v_add_u32_e32 v178, 0x8800, v1
	v_add_u32_e32 v179, 0x9000, v1
	v_add_u32_e32 v180, 0xa000, v1
	v_add_u32_e32 v181, 0xa800, v1
	v_add_u32_e32 v182, 0xb000, v1
	v_add_u32_e32 v183, 0xc400, v1
	v_add_u32_e32 v184, 0xc800, v1
	v_add_u32_e32 v185, 0xcc00, v1
	v_add_u32_e32 v186, 0xd000, v1
	v_add_u32_e32 v187, 0xe400, v1
	v_add_u32_e32 v188, 0xe800, v1
	v_add_u32_e32 v189, 0xec00, v1
	v_add_u32_e32 v190, 0xf000, v1
	s_mov_b32 s41, 0
	s_barrier
	s_barrier
	s_branch .LBB1_145

.LBB1_145:
	s_lshl_b32 s39, s41, 15
	s_mov_b64 s[42:43], s[20:21]
	s_mov_b64 s[44:45], s[16:17]
	s_add_i32 s40, s39, 0x8000
	s_add_i32 s2, s40, s11
	s_lshl_b64 s[44:45], s[2:3], 10
	v_lshl_add_u64 v[130:131], s[42:43], 0, v[162:163]
	s_or_b32 s42, s2, 1
	s_mov_b32 s43, s3
	v_lshl_add_u64 v[132:133], v[130:131], 0, s[44:45]
	s_lshl_b64 s[42:43], s[42:43], 10
	s_waitcnt vmcnt(31)
	global_store_dwordx4 v[132:133], v[126:129], off nt
	s_lshl_b32 s41, s41, 25
	s_mov_b64 s[44:45], s[16:17]
	v_cvt_pk_f16_f32 v129, v128, v129
	v_cvt_pk_f16_f32 v128, v126, v127
	v_lshl_add_u64 v[126:127], v[130:131], 0, s[42:43]
	s_or_b32 s42, s2, 2
	s_mov_b32 s43, s3
	s_lshl_b64 s[42:43], s[42:43], 10
	s_waitcnt vmcnt(31)
	global_store_dwordx4 v[126:127], v[122:125], off nt
	s_nop 1
	v_cvt_pk_f16_f32 v125, v124, v125
	v_cvt_pk_f16_f32 v124, v122, v123
	v_lshl_add_u64 v[122:123], v[130:131], 0, s[42:43]
	s_or_b32 s42, s2, 3
	s_mov_b32 s43, s3
	s_lshl_b64 s[42:43], s[42:43], 10
	s_waitcnt vmcnt(31)
	global_store_dwordx4 v[122:123], v[118:121], off nt
	ds_write2_b64 v1, v[128:129], v[124:125] offset1:66
	s_nop 0
	v_cvt_pk_f16_f32 v121, v120, v121
	v_cvt_pk_f16_f32 v120, v118, v119
	v_lshl_add_u64 v[118:119], v[130:131], 0, s[42:43]
	s_or_b32 s42, s2, 4
	s_mov_b32 s43, s3
	s_lshl_b64 s[42:43], s[42:43], 10
	s_waitcnt vmcnt(31)
	global_store_dwordx4 v[118:119], v[114:117], off nt
	s_nop 1
	v_cvt_pk_f16_f32 v117, v116, v117
	v_cvt_pk_f16_f32 v116, v114, v115
	v_lshl_add_u64 v[114:115], v[130:131], 0, s[42:43]
	s_or_b32 s42, s2, 5
	s_mov_b32 s43, s3
	s_lshl_b64 s[42:43], s[42:43], 10
	s_waitcnt vmcnt(31)
	global_store_dwordx4 v[114:115], v[110:113], off nt
	ds_write2_b64 v1, v[120:121], v[116:117] offset0:132 offset1:198
	s_nop 0
	v_cvt_pk_f16_f32 v113, v112, v113
	v_cvt_pk_f16_f32 v112, v110, v111
	v_lshl_add_u64 v[110:111], v[130:131], 0, s[42:43]
	s_or_b32 s42, s2, 6
	s_mov_b32 s43, s3
	s_lshl_b64 s[42:43], s[42:43], 10
	s_or_b32 s2, s2, 7
	s_waitcnt vmcnt(31)
	global_store_dwordx4 v[110:111], v[106:109], off nt
	s_nop 1
	v_cvt_pk_f16_f32 v109, v108, v109
	v_cvt_pk_f16_f32 v108, v106, v107
	v_lshl_add_u64 v[106:107], v[130:131], 0, s[42:43]
	s_lshl_b64 s[42:43], s[2:3], 10
	s_waitcnt vmcnt(31)
	global_store_dwordx4 v[106:107], v[102:105], off nt
	s_add_i32 s2, s41, s34
	s_or_b32 s2, s2, s10
	v_cvt_pk_f16_f32 v105, v104, v105
	v_cvt_pk_f16_f32 v104, v102, v103
	v_lshl_add_u64 v[102:103], v[130:131], 0, s[42:43]
	s_waitcnt vmcnt(31)
	global_store_dwordx4 v[102:103], v[94:97], off nt
	ds_write2_b64 v166, v[112:113], v[108:109] offset0:8 offset1:74
	s_or_b32 s42, s2, 0x400
	v_cvt_pk_f16_f32 v97, v96, v97
	v_cvt_pk_f16_f32 v96, v94, v95
	ds_write2_b64 v166, v[104:105], v[96:97] offset0:140 offset1:206
	buffer_load_dwordx4 v[126:129], v162, s[4:7], s2 offen nt sc1
	buffer_load_dwordx4 v[122:125], v162, s[4:7], s42 offen nt sc1
	s_or_b32 s42, s2, 0x800
	s_or_b32 s43, s2, 0xc00
	buffer_load_dwordx4 v[118:121], v162, s[4:7], s42 offen nt sc1
	buffer_load_dwordx4 v[114:117], v162, s[4:7], s43 offen nt sc1
	s_or_b32 s42, s2, 0x1000
	s_or_b32 s43, s2, 0x1400
	buffer_load_dwordx4 v[110:113], v162, s[4:7], s42 offen nt sc1
	buffer_load_dwordx4 v[106:109], v162, s[4:7], s43 offen nt sc1
	s_or_b32 s42, s2, 0x1800
	s_or_b32 s2, s2, 0x1c00
	buffer_load_dwordx4 v[102:105], v162, s[4:7], s42 offen nt sc1
	buffer_load_dwordx4 v[94:97], v162, s[4:7], s2 offen nt sc1
	s_mov_b64 s[42:43], s[20:21]
	s_waitcnt lgkmcnt(0)
	s_barrier
	s_add_i32 s2, s22, s40
	s_lshl_b64 s[44:45], s[2:3], 10
	v_lshl_add_u64 v[130:131], s[42:43], 0, v[162:163]
	s_or_b32 s42, s2, 1
	s_mov_b32 s43, s3
	v_lshl_add_u64 v[132:133], v[130:131], 0, s[44:45]
	s_lshl_b64 s[42:43], s[42:43], 10
	s_waitcnt vmcnt(39)
	global_store_dwordx4 v[132:133], v[98:101], off nt
	s_mov_b64 s[44:45], s[16:17]
	s_nop 0
	v_cvt_pk_f16_f32 v101, v100, v101
	v_cvt_pk_f16_f32 v100, v98, v99
	v_lshl_add_u64 v[98:99], v[130:131], 0, s[42:43]
	s_or_b32 s42, s2, 2
	s_mov_b32 s43, s3
	s_lshl_b64 s[42:43], s[42:43], 10
	s_waitcnt vmcnt(39)
	global_store_dwordx4 v[98:99], v[90:93], off nt
	s_nop 1
	v_cvt_pk_f16_f32 v93, v92, v93
	v_cvt_pk_f16_f32 v92, v90, v91
	v_lshl_add_u64 v[90:91], v[130:131], 0, s[42:43]
	s_or_b32 s42, s2, 3
	s_mov_b32 s43, s3
	s_lshl_b64 s[42:43], s[42:43], 10
	s_waitcnt vmcnt(39)
	global_store_dwordx4 v[90:91], v[86:89], off nt
	ds_write2_b64 v167, v[100:101], v[92:93] offset0:32 offset1:98
	s_nop 0
	v_cvt_pk_f16_f32 v89, v88, v89
	v_cvt_pk_f16_f32 v88, v86, v87
	v_lshl_add_u64 v[86:87], v[130:131], 0, s[42:43]
	s_or_b32 s42, s2, 4
	s_mov_b32 s43, s3
	s_lshl_b64 s[42:43], s[42:43], 10
	s_waitcnt vmcnt(39)
	global_store_dwordx4 v[86:87], v[82:85], off nt
	s_nop 1
	v_cvt_pk_f16_f32 v85, v84, v85
	v_cvt_pk_f16_f32 v84, v82, v83
	v_lshl_add_u64 v[82:83], v[130:131], 0, s[42:43]
	s_or_b32 s42, s2, 5
	s_mov_b32 s43, s3
	s_lshl_b64 s[42:43], s[42:43], 10
	s_waitcnt vmcnt(39)
	global_store_dwordx4 v[82:83], v[78:81], off nt
	ds_write2_b64 v167, v[88:89], v[84:85] offset0:164 offset1:230
	s_nop 0
	v_cvt_pk_f16_f32 v81, v80, v81
	v_cvt_pk_f16_f32 v80, v78, v79
	v_lshl_add_u64 v[78:79], v[130:131], 0, s[42:43]
	s_or_b32 s42, s2, 6
	s_mov_b32 s43, s3
	s_lshl_b64 s[42:43], s[42:43], 10
	s_or_b32 s2, s2, 7
	s_waitcnt vmcnt(39)
	global_store_dwordx4 v[78:79], v[74:77], off nt
	s_nop 1
	v_cvt_pk_f16_f32 v77, v76, v77
	v_cvt_pk_f16_f32 v76, v74, v75
	v_lshl_add_u64 v[74:75], v[130:131], 0, s[42:43]
	s_lshl_b64 s[42:43], s[2:3], 10
	s_waitcnt vmcnt(39)
	global_store_dwordx4 v[74:75], v[66:69], off nt
	s_add_i32 s2, s41, s35
	ds_write2_b64 v168, v[80:81], v[76:77] offset0:40 offset1:106
	v_cvt_pk_f16_f32 v69, v68, v69
	v_cvt_pk_f16_f32 v68, v66, v67
	v_lshl_add_u64 v[66:67], v[130:131], 0, s[42:43]
	s_waitcnt vmcnt(39)
	global_store_dwordx4 v[66:67], v[58:61], off nt
	s_or_b32 s2, s2, s10
	s_or_b32 s42, s2, 0x400
	v_cvt_pk_f16_f32 v61, v60, v61
	v_cvt_pk_f16_f32 v60, v58, v59
	ds_write2_b64 v168, v[68:69], v[60:61] offset0:172 offset1:238
	buffer_load_dwordx4 v[98:101], v162, s[4:7], s2 offen nt sc1
	buffer_load_dwordx4 v[90:93], v162, s[4:7], s42 offen nt sc1
	s_or_b32 s42, s2, 0x800
	s_or_b32 s43, s2, 0xc00
	buffer_load_dwordx4 v[86:89], v162, s[4:7], s42 offen nt sc1
	buffer_load_dwordx4 v[82:85], v162, s[4:7], s43 offen nt sc1
	s_or_b32 s42, s2, 0x1000
	s_or_b32 s43, s2, 0x1400
	buffer_load_dwordx4 v[78:81], v162, s[4:7], s42 offen nt sc1
	buffer_load_dwordx4 v[74:77], v162, s[4:7], s43 offen nt sc1
	s_or_b32 s42, s2, 0x1800
	s_or_b32 s2, s2, 0x1c00
	buffer_load_dwordx4 v[66:69], v162, s[4:7], s42 offen nt sc1
	buffer_load_dwordx4 v[58:61], v162, s[4:7], s2 offen nt sc1
	s_mov_b64 s[42:43], s[20:21]
	s_waitcnt lgkmcnt(0)
	s_barrier
	s_add_i32 s2, s23, s40
	s_lshl_b64 s[44:45], s[2:3], 10
	v_lshl_add_u64 v[130:131], s[42:43], 0, v[162:163]
	s_or_b32 s42, s2, 1
	s_mov_b32 s43, s3
	v_lshl_add_u64 v[132:133], v[130:131], 0, s[44:45]
	s_lshl_b64 s[42:43], s[42:43], 10
	s_waitcnt vmcnt(47)
	global_store_dwordx4 v[132:133], v[70:73], off nt
	s_mov_b64 s[44:45], s[16:17]
	s_nop 0
	v_cvt_pk_f16_f32 v73, v72, v73
	v_cvt_pk_f16_f32 v72, v70, v71
	v_lshl_add_u64 v[70:71], v[130:131], 0, s[42:43]
	s_or_b32 s42, s2, 2
	s_mov_b32 s43, s3
	s_lshl_b64 s[42:43], s[42:43], 10
	s_waitcnt vmcnt(47)
	global_store_dwordx4 v[70:71], v[62:65], off nt
	s_nop 1
	v_cvt_pk_f16_f32 v65, v64, v65
	v_cvt_pk_f16_f32 v64, v62, v63
	v_lshl_add_u64 v[62:63], v[130:131], 0, s[42:43]
	s_or_b32 s42, s2, 3
	s_mov_b32 s43, s3
	s_lshl_b64 s[42:43], s[42:43], 10
	s_waitcnt vmcnt(47)
	global_store_dwordx4 v[62:63], v[54:57], off nt
	ds_write2_b64 v169, v[72:73], v[64:65] offset0:64 offset1:130
	s_nop 0
	v_cvt_pk_f16_f32 v57, v56, v57
	v_cvt_pk_f16_f32 v56, v54, v55
	v_lshl_add_u64 v[54:55], v[130:131], 0, s[42:43]
	s_or_b32 s42, s2, 4
	s_mov_b32 s43, s3
	s_lshl_b64 s[42:43], s[42:43], 10
	s_waitcnt vmcnt(47)
	global_store_dwordx4 v[54:55], v[50:53], off nt
	s_nop 1
	v_cvt_pk_f16_f32 v53, v52, v53
	v_cvt_pk_f16_f32 v52, v50, v51
	v_lshl_add_u64 v[50:51], v[130:131], 0, s[42:43]
	s_or_b32 s42, s2, 5
	s_mov_b32 s43, s3
	s_lshl_b64 s[42:43], s[42:43], 10
	s_waitcnt vmcnt(47)
	global_store_dwordx4 v[50:51], v[46:49], off nt
	ds_write2_b64 v170, v[56:57], v[52:53] offset0:68 offset1:134
	s_nop 0
	v_cvt_pk_f16_f32 v49, v48, v49
	v_cvt_pk_f16_f32 v48, v46, v47
	v_lshl_add_u64 v[46:47], v[130:131], 0, s[42:43]
	s_or_b32 s42, s2, 6
	s_mov_b32 s43, s3
	s_lshl_b64 s[42:43], s[42:43], 10
	s_or_b32 s2, s2, 7
	s_waitcnt vmcnt(47)
	global_store_dwordx4 v[46:47], v[42:45], off nt
	s_nop 1
	v_cvt_pk_f16_f32 v45, v44, v45
	v_cvt_pk_f16_f32 v44, v42, v43
	v_lshl_add_u64 v[42:43], v[130:131], 0, s[42:43]
	s_lshl_b64 s[42:43], s[2:3], 10
	s_waitcnt vmcnt(47)
	global_store_dwordx4 v[42:43], v[34:37], off nt
	s_add_i32 s2, s41, s36
	ds_write2_b64 v171, v[48:49], v[44:45] offset0:72 offset1:138
	v_cvt_pk_f16_f32 v37, v36, v37
	v_cvt_pk_f16_f32 v36, v34, v35
	v_lshl_add_u64 v[34:35], v[130:131], 0, s[42:43]
	s_waitcnt vmcnt(47)
	global_store_dwordx4 v[34:35], v[26:29], off nt
	s_or_b32 s2, s2, s10
	s_or_b32 s42, s2, 0x400
	v_cvt_pk_f16_f32 v29, v28, v29
	v_cvt_pk_f16_f32 v28, v26, v27
	ds_write2_b64 v172, v[36:37], v[28:29] offset0:76 offset1:142
	buffer_load_dwordx4 v[70:73], v162, s[4:7], s2 offen nt sc1
	buffer_load_dwordx4 v[62:65], v162, s[4:7], s42 offen nt sc1
	s_or_b32 s42, s2, 0x800
	s_or_b32 s43, s2, 0xc00
	buffer_load_dwordx4 v[54:57], v162, s[4:7], s42 offen nt sc1
	buffer_load_dwordx4 v[50:53], v162, s[4:7], s43 offen nt sc1
	s_or_b32 s42, s2, 0x1000
	s_or_b32 s43, s2, 0x1400
	buffer_load_dwordx4 v[46:49], v162, s[4:7], s42 offen nt sc1
	buffer_load_dwordx4 v[42:45], v162, s[4:7], s43 offen nt sc1
	s_or_b32 s42, s2, 0x1800
	s_or_b32 s2, s2, 0x1c00
	buffer_load_dwordx4 v[34:37], v162, s[4:7], s42 offen nt sc1
	buffer_load_dwordx4 v[26:29], v162, s[4:7], s2 offen nt sc1
	s_mov_b64 s[42:43], s[20:21]
	s_waitcnt lgkmcnt(0)
	s_barrier
	s_add_i32 s2, s24, s40
	s_lshl_b64 s[44:45], s[2:3], 10
	v_lshl_add_u64 v[130:131], s[42:43], 0, v[162:163]
	s_or_b32 s42, s2, 1
	s_mov_b32 s43, s3
	v_lshl_add_u64 v[132:133], v[130:131], 0, s[44:45]
	s_lshl_b64 s[42:43], s[42:43], 10
	s_waitcnt vmcnt(55)
	global_store_dwordx4 v[132:133], v[38:41], off nt
	s_mov_b64 s[44:45], s[16:17]
	s_nop 0
	v_cvt_pk_f16_f32 v41, v40, v41
	v_cvt_pk_f16_f32 v40, v38, v39
	v_lshl_add_u64 v[38:39], v[130:131], 0, s[42:43]
	s_or_b32 s42, s2, 2
	s_mov_b32 s43, s3
	s_lshl_b64 s[42:43], s[42:43], 10
	s_waitcnt vmcnt(55)
	global_store_dwordx4 v[38:39], v[30:33], off nt
	s_nop 1
	v_cvt_pk_f16_f32 v33, v32, v33
	v_cvt_pk_f16_f32 v32, v30, v31
	v_lshl_add_u64 v[30:31], v[130:131], 0, s[42:43]
	s_or_b32 s42, s2, 3
	s_mov_b32 s43, s3
	s_lshl_b64 s[42:43], s[42:43], 10
	s_waitcnt vmcnt(55)
	global_store_dwordx4 v[30:31], v[22:25], off nt
	ds_write2_b64 v173, v[40:41], v[32:33] offset0:96 offset1:162
	s_nop 0
	v_cvt_pk_f16_f32 v25, v24, v25
	v_cvt_pk_f16_f32 v24, v22, v23
	v_lshl_add_u64 v[22:23], v[130:131], 0, s[42:43]
	s_or_b32 s42, s2, 4
	s_mov_b32 s43, s3
	s_lshl_b64 s[42:43], s[42:43], 10
	s_waitcnt vmcnt(55)
	global_store_dwordx4 v[22:23], v[18:21], off nt
	s_nop 1
	v_cvt_pk_f16_f32 v21, v20, v21
	v_cvt_pk_f16_f32 v20, v18, v19
	v_lshl_add_u64 v[18:19], v[130:131], 0, s[42:43]
	s_or_b32 s42, s2, 5
	s_mov_b32 s43, s3
	s_lshl_b64 s[42:43], s[42:43], 10
	s_waitcnt vmcnt(55)
	global_store_dwordx4 v[18:19], v[14:17], off nt
	ds_write2_b64 v174, v[24:25], v[20:21] offset0:100 offset1:166
	s_nop 0
	v_cvt_pk_f16_f32 v17, v16, v17
	v_cvt_pk_f16_f32 v16, v14, v15
	v_lshl_add_u64 v[14:15], v[130:131], 0, s[42:43]
	s_or_b32 s42, s2, 6
	s_mov_b32 s43, s3
	s_lshl_b64 s[42:43], s[42:43], 10
	s_or_b32 s2, s2, 7
	s_waitcnt vmcnt(55)
	global_store_dwordx4 v[14:15], v[10:13], off nt
	s_nop 1
	v_cvt_pk_f16_f32 v13, v12, v13
	v_cvt_pk_f16_f32 v12, v10, v11
	v_lshl_add_u64 v[10:11], v[130:131], 0, s[42:43]
	s_lshl_b64 s[42:43], s[2:3], 10
	s_waitcnt vmcnt(55)
	global_store_dwordx4 v[10:11], v[6:9], off nt
	s_add_i32 s2, s41, s37
	ds_write2_b64 v175, v[16:17], v[12:13] offset0:104 offset1:170
	v_cvt_pk_f16_f32 v9, v8, v9
	v_cvt_pk_f16_f32 v8, v6, v7
	v_lshl_add_u64 v[6:7], v[130:131], 0, s[42:43]
	s_waitcnt vmcnt(55)
	global_store_dwordx4 v[6:7], v[2:5], off nt
	s_or_b32 s2, s2, s10
	s_or_b32 s42, s2, 0x400
	v_cvt_pk_f16_f32 v5, v4, v5
	v_cvt_pk_f16_f32 v4, v2, v3
	ds_write2_b64 v176, v[8:9], v[4:5] offset0:108 offset1:174
	buffer_load_dwordx4 v[146:149], v162, s[4:7], s2 offen nt sc1
	buffer_load_dwordx4 v[130:133], v162, s[4:7], s42 offen nt sc1
	s_or_b32 s42, s2, 0x800
	s_or_b32 s43, s2, 0xc00
	buffer_load_dwordx4 v[150:153], v162, s[4:7], s42 offen nt sc1
	buffer_load_dwordx4 v[134:137], v162, s[4:7], s43 offen nt sc1
	s_or_b32 s42, s2, 0x1000
	s_or_b32 s43, s2, 0x1400
	buffer_load_dwordx4 v[154:157], v162, s[4:7], s42 offen nt sc1
	buffer_load_dwordx4 v[138:141], v162, s[4:7], s43 offen nt sc1
	s_or_b32 s42, s2, 0x1800
	s_or_b32 s2, s2, 0x1c00
	buffer_load_dwordx4 v[158:161], v162, s[4:7], s42 offen nt sc1
	buffer_load_dwordx4 v[142:145], v162, s[4:7], s2 offen nt sc1
	s_mov_b64 s[42:43], s[20:21]
	s_waitcnt lgkmcnt(0)
	s_barrier
	s_add_i32 s2, s25, s40
	v_lshl_add_u64 v[2:3], s[42:43], 0, v[162:163]
	s_or_b32 s42, s2, 1
	s_mov_b32 s43, s3
	s_lshl_b64 s[44:45], s[2:3], 10
	s_lshl_b64 s[42:43], s[42:43], 10
	v_lshl_add_u64 v[4:5], v[2:3], 0, s[44:45]
	v_lshl_add_u64 v[6:7], v[2:3], 0, s[42:43]
	s_or_b32 s42, s2, 2
	s_mov_b32 s43, s3
	s_waitcnt vmcnt(55)
	global_store_dwordx4 v[4:5], v[126:129], off nt
	v_cvt_pk_f16_f32 v5, v128, v129
	v_cvt_pk_f16_f32 v4, v126, v127
	s_waitcnt vmcnt(55)
	global_store_dwordx4 v[6:7], v[122:125], off nt
	v_cvt_pk_f16_f32 v7, v124, v125
	v_cvt_pk_f16_f32 v6, v122, v123
	s_lshl_b64 s[42:43], s[42:43], 10
	ds_write2_b64 v177, v[4:5], v[6:7] offset0:128 offset1:194
	v_lshl_add_u64 v[4:5], v[2:3], 0, s[42:43]
	s_or_b32 s42, s2, 3
	s_mov_b32 s43, s3
	s_lshl_b64 s[42:43], s[42:43], 10
	v_lshl_add_u64 v[6:7], v[2:3], 0, s[42:43]
	s_or_b32 s42, s2, 4
	s_mov_b32 s43, s3
	s_waitcnt vmcnt(55)
	global_store_dwordx4 v[4:5], v[118:121], off nt
	v_cvt_pk_f16_f32 v5, v120, v121
	v_cvt_pk_f16_f32 v4, v118, v119
	s_waitcnt vmcnt(55)
	global_store_dwordx4 v[6:7], v[114:117], off nt
	v_cvt_pk_f16_f32 v7, v116, v117
	v_cvt_pk_f16_f32 v6, v114, v115
	s_lshl_b64 s[42:43], s[42:43], 10
	ds_write2_b64 v178, v[4:5], v[6:7] offset0:4 offset1:70
	v_lshl_add_u64 v[4:5], v[2:3], 0, s[42:43]
	s_or_b32 s42, s2, 5
	s_mov_b32 s43, s3
	s_lshl_b64 s[42:43], s[42:43], 10
	v_lshl_add_u64 v[6:7], v[2:3], 0, s[42:43]
	s_or_b32 s42, s2, 6
	s_mov_b32 s43, s3
	s_waitcnt vmcnt(55)
	global_store_dwordx4 v[4:5], v[110:113], off nt
	v_cvt_pk_f16_f32 v5, v112, v113
	v_cvt_pk_f16_f32 v4, v110, v111
	s_waitcnt vmcnt(55)
	global_store_dwordx4 v[6:7], v[106:109], off nt
	v_cvt_pk_f16_f32 v7, v108, v109
	v_cvt_pk_f16_f32 v6, v106, v107
	s_lshl_b64 s[42:43], s[42:43], 10
	s_or_b32 s2, s2, 7
	ds_write2_b64 v178, v[4:5], v[6:7] offset0:136 offset1:202
	v_lshl_add_u64 v[4:5], v[2:3], 0, s[42:43]
	s_lshl_b64 s[42:43], s[2:3], 10
	v_lshl_add_u64 v[2:3], v[2:3], 0, s[42:43]
	s_add_i32 s41, s41, s38
	s_waitcnt vmcnt(55)
	global_store_dwordx4 v[4:5], v[102:105], off nt
	v_cvt_pk_f16_f32 v5, v104, v105
	v_cvt_pk_f16_f32 v4, v102, v103
	s_waitcnt vmcnt(55)
	global_store_dwordx4 v[2:3], v[94:97], off nt
	v_cvt_pk_f16_f32 v3, v96, v97
	v_cvt_pk_f16_f32 v2, v94, v95
	s_or_b32 s2, s41, s10
	ds_write2_b64 v179, v[4:5], v[2:3] offset0:12 offset1:78
	s_or_b32 s41, s2, 0x400
	buffer_load_dwordx4 v[126:129], v162, s[4:7], s2 offen nt sc1
	buffer_load_dwordx4 v[122:125], v162, s[4:7], s41 offen nt sc1
	s_or_b32 s41, s2, 0x800
	s_or_b32 s42, s2, 0xc00
	buffer_load_dwordx4 v[118:121], v162, s[4:7], s41 offen nt sc1
	buffer_load_dwordx4 v[114:117], v162, s[4:7], s42 offen nt sc1
	s_or_b32 s41, s2, 0x1000
	s_or_b32 s42, s2, 0x1400
	buffer_load_dwordx4 v[110:113], v162, s[4:7], s41 offen nt sc1
	buffer_load_dwordx4 v[106:109], v162, s[4:7], s42 offen nt sc1
	s_or_b32 s41, s2, 0x1800
	s_or_b32 s2, s2, 0x1c00
	s_mov_b64 s[42:43], s[20:21]
	s_mov_b64 s[44:45], s[16:17]
	buffer_load_dwordx4 v[102:105], v162, s[4:7], s41 offen nt sc1
	buffer_load_dwordx4 v[94:97], v162, s[4:7], s2 offen nt sc1
	s_waitcnt lgkmcnt(0)
	s_barrier
	s_add_i32 s2, s26, s40
	v_lshl_add_u64 v[2:3], s[42:43], 0, v[162:163]
	s_or_b32 s42, s2, 1
	s_mov_b32 s43, s3
	s_lshl_b64 s[44:45], s[2:3], 10
	s_lshl_b64 s[42:43], s[42:43], 10
	v_lshl_add_u64 v[4:5], v[2:3], 0, s[44:45]
	v_lshl_add_u64 v[6:7], v[2:3], 0, s[42:43]
	s_or_b32 s42, s2, 2
	s_mov_b32 s43, s3
	s_waitcnt vmcnt(55)
	global_store_dwordx4 v[4:5], v[98:101], off nt
	v_cvt_pk_f16_f32 v5, v100, v101
	v_cvt_pk_f16_f32 v4, v98, v99
	s_waitcnt vmcnt(55)
	global_store_dwordx4 v[6:7], v[90:93], off nt
	v_cvt_pk_f16_f32 v7, v92, v93
	v_cvt_pk_f16_f32 v6, v90, v91
	s_lshl_b64 s[42:43], s[42:43], 10
	ds_write2_b64 v180, v[4:5], v[6:7] offset0:160 offset1:226
	v_lshl_add_u64 v[4:5], v[2:3], 0, s[42:43]
	s_or_b32 s42, s2, 3
	s_mov_b32 s43, s3
	s_lshl_b64 s[42:43], s[42:43], 10
	v_lshl_add_u64 v[6:7], v[2:3], 0, s[42:43]
	s_or_b32 s42, s2, 4
	s_mov_b32 s43, s3
	s_waitcnt vmcnt(55)
	global_store_dwordx4 v[4:5], v[86:89], off nt
	v_cvt_pk_f16_f32 v5, v88, v89
	v_cvt_pk_f16_f32 v4, v86, v87
	s_waitcnt vmcnt(55)
	global_store_dwordx4 v[6:7], v[82:85], off nt
	v_cvt_pk_f16_f32 v7, v84, v85
	v_cvt_pk_f16_f32 v6, v82, v83
	s_lshl_b64 s[42:43], s[42:43], 10
	ds_write2_b64 v181, v[4:5], v[6:7] offset0:36 offset1:102
	v_lshl_add_u64 v[4:5], v[2:3], 0, s[42:43]
	s_or_b32 s42, s2, 5
	s_mov_b32 s43, s3
	s_lshl_b64 s[42:43], s[42:43], 10
	v_lshl_add_u64 v[6:7], v[2:3], 0, s[42:43]
	s_or_b32 s42, s2, 6
	s_mov_b32 s43, s3
	s_waitcnt vmcnt(55)
	global_store_dwordx4 v[4:5], v[78:81], off nt
	v_cvt_pk_f16_f32 v5, v80, v81
	v_cvt_pk_f16_f32 v4, v78, v79
	s_waitcnt vmcnt(55)
	global_store_dwordx4 v[6:7], v[74:77], off nt
	v_cvt_pk_f16_f32 v7, v76, v77
	v_cvt_pk_f16_f32 v6, v74, v75
	s_lshl_b64 s[42:43], s[42:43], 10
	s_or_b32 s2, s2, 7
	ds_write2_b64 v181, v[4:5], v[6:7] offset0:168 offset1:234
	v_lshl_add_u64 v[4:5], v[2:3], 0, s[42:43]
	s_lshl_b64 s[42:43], s[2:3], 10
	s_add_i32 s2, s39, 0x9000
	s_and_b32 s2, s2, 0x18000
	s_add_i32 s2, s27, s2
	v_lshl_add_u64 v[2:3], v[2:3], 0, s[42:43]
	s_lshl_b32 s2, s2, 10
	s_waitcnt vmcnt(55)
	global_store_dwordx4 v[4:5], v[66:69], off nt
	v_cvt_pk_f16_f32 v5, v68, v69
	v_cvt_pk_f16_f32 v4, v66, v67
	s_waitcnt vmcnt(55)
	global_store_dwordx4 v[2:3], v[58:61], off nt
	v_cvt_pk_f16_f32 v3, v60, v61
	v_cvt_pk_f16_f32 v2, v58, v59
	s_or_b32 s2, s2, s10
	ds_write2_b64 v182, v[4:5], v[2:3] offset0:44 offset1:110
	s_or_b32 s41, s2, 0x400
	buffer_load_dwordx4 v[98:101], v162, s[4:7], s2 offen nt sc1
	buffer_load_dwordx4 v[90:93], v162, s[4:7], s41 offen nt sc1
	s_or_b32 s41, s2, 0x800
	s_or_b32 s42, s2, 0xc00
	buffer_load_dwordx4 v[86:89], v162, s[4:7], s41 offen nt sc1
	buffer_load_dwordx4 v[82:85], v162, s[4:7], s42 offen nt sc1
	s_or_b32 s41, s2, 0x1000
	s_or_b32 s42, s2, 0x1400
	buffer_load_dwordx4 v[78:81], v162, s[4:7], s41 offen nt sc1
	buffer_load_dwordx4 v[74:77], v162, s[4:7], s42 offen nt sc1
	s_or_b32 s41, s2, 0x1800
	s_or_b32 s2, s2, 0x1c00
	s_mov_b64 s[42:43], s[20:21]
	s_mov_b64 s[44:45], s[16:17]
	buffer_load_dwordx4 v[66:69], v162, s[4:7], s41 offen nt sc1
	buffer_load_dwordx4 v[58:61], v162, s[4:7], s2 offen nt sc1
	s_waitcnt lgkmcnt(0)
	s_barrier
	s_add_i32 s2, s28, s40
	v_lshl_add_u64 v[2:3], s[42:43], 0, v[162:163]
	s_or_b32 s42, s2, 1
	s_mov_b32 s43, s3
	s_lshl_b64 s[44:45], s[2:3], 10
	s_lshl_b64 s[42:43], s[42:43], 10
	v_lshl_add_u64 v[4:5], v[2:3], 0, s[44:45]
	v_lshl_add_u64 v[6:7], v[2:3], 0, s[42:43]
	s_or_b32 s42, s2, 2
	s_mov_b32 s43, s3
	s_waitcnt vmcnt(55)
	global_store_dwordx4 v[4:5], v[70:73], off nt
	v_cvt_pk_f16_f32 v5, v72, v73
	v_cvt_pk_f16_f32 v4, v70, v71
	s_waitcnt vmcnt(55)
	global_store_dwordx4 v[6:7], v[62:65], off nt
	v_cvt_pk_f16_f32 v7, v64, v65
	v_cvt_pk_f16_f32 v6, v62, v63
	s_lshl_b64 s[42:43], s[42:43], 10
	ds_write2_b64 v183, v[4:5], v[6:7] offset0:64 offset1:130
	v_lshl_add_u64 v[4:5], v[2:3], 0, s[42:43]
	s_or_b32 s42, s2, 3
	s_mov_b32 s43, s3
	s_lshl_b64 s[42:43], s[42:43], 10
	v_lshl_add_u64 v[6:7], v[2:3], 0, s[42:43]
	s_or_b32 s42, s2, 4
	s_mov_b32 s43, s3
	s_waitcnt vmcnt(55)
	global_store_dwordx4 v[4:5], v[54:57], off nt
	v_cvt_pk_f16_f32 v5, v56, v57
	v_cvt_pk_f16_f32 v4, v54, v55
	s_waitcnt vmcnt(55)
	global_store_dwordx4 v[6:7], v[50:53], off nt
	v_cvt_pk_f16_f32 v7, v52, v53
	v_cvt_pk_f16_f32 v6, v50, v51
	s_lshl_b64 s[42:43], s[42:43], 10
	ds_write2_b64 v184, v[4:5], v[6:7] offset0:68 offset1:134
	v_lshl_add_u64 v[4:5], v[2:3], 0, s[42:43]
	s_or_b32 s42, s2, 5
	s_mov_b32 s43, s3
	s_lshl_b64 s[42:43], s[42:43], 10
	v_lshl_add_u64 v[6:7], v[2:3], 0, s[42:43]
	s_or_b32 s42, s2, 6
	s_mov_b32 s43, s3
	s_waitcnt vmcnt(55)
	global_store_dwordx4 v[4:5], v[46:49], off nt
	v_cvt_pk_f16_f32 v5, v48, v49
	v_cvt_pk_f16_f32 v4, v46, v47
	s_waitcnt vmcnt(55)
	global_store_dwordx4 v[6:7], v[42:45], off nt
	v_cvt_pk_f16_f32 v7, v44, v45
	v_cvt_pk_f16_f32 v6, v42, v43
	s_lshl_b64 s[42:43], s[42:43], 10
	s_or_b32 s2, s2, 7
	ds_write2_b64 v185, v[4:5], v[6:7] offset0:72 offset1:138
	v_lshl_add_u64 v[4:5], v[2:3], 0, s[42:43]
	s_lshl_b64 s[42:43], s[2:3], 10
	s_add_i32 s2, s39, 0xa000
	s_and_b32 s2, s2, 0x18000
	s_add_i32 s2, s29, s2
	v_lshl_add_u64 v[2:3], v[2:3], 0, s[42:43]
	s_lshl_b32 s2, s2, 10
	s_waitcnt vmcnt(55)
	global_store_dwordx4 v[4:5], v[34:37], off nt
	v_cvt_pk_f16_f32 v5, v36, v37
	v_cvt_pk_f16_f32 v4, v34, v35
	s_waitcnt vmcnt(55)
	global_store_dwordx4 v[2:3], v[26:29], off nt
	v_cvt_pk_f16_f32 v3, v28, v29
	v_cvt_pk_f16_f32 v2, v26, v27
	s_or_b32 s2, s2, s10
	ds_write2_b64 v186, v[4:5], v[2:3] offset0:76 offset1:142
	s_or_b32 s41, s2, 0x400
	buffer_load_dwordx4 v[70:73], v162, s[4:7], s2 offen nt sc1
	buffer_load_dwordx4 v[62:65], v162, s[4:7], s41 offen nt sc1
	s_or_b32 s41, s2, 0x800
	s_or_b32 s42, s2, 0xc00
	buffer_load_dwordx4 v[54:57], v162, s[4:7], s41 offen nt sc1
	buffer_load_dwordx4 v[50:53], v162, s[4:7], s42 offen nt sc1
	s_or_b32 s41, s2, 0x1000
	s_or_b32 s42, s2, 0x1400
	buffer_load_dwordx4 v[46:49], v162, s[4:7], s41 offen nt sc1
	buffer_load_dwordx4 v[42:45], v162, s[4:7], s42 offen nt sc1
	s_or_b32 s41, s2, 0x1800
	s_or_b32 s2, s2, 0x1c00
	buffer_load_dwordx4 v[34:37], v162, s[4:7], s41 offen nt sc1
	buffer_load_dwordx4 v[26:29], v162, s[4:7], s2 offen nt sc1
	s_mov_b64 s[42:43], s[20:21]
	s_mov_b64 s[44:45], s[16:17]
	s_add_i32 s2, s30, s40
	s_waitcnt lgkmcnt(0)
	s_barrier
	s_lshl_b64 s[40:41], s[2:3], 10
	v_lshl_add_u64 v[2:3], s[42:43], 0, v[162:163]
	v_lshl_add_u64 v[4:5], v[2:3], 0, s[40:41]
	s_or_b32 s40, s2, 1
	s_mov_b32 s41, s3
	s_lshl_b64 s[40:41], s[40:41], 10
	s_waitcnt vmcnt(55)
	global_store_dwordx4 v[4:5], v[146:149], off nt
	v_lshl_add_u64 v[4:5], v[2:3], 0, s[40:41]
	s_or_b32 s40, s2, 2
	s_mov_b32 s41, s3
	s_lshl_b64 s[40:41], s[40:41], 10
	s_waitcnt vmcnt(55)
	global_store_dwordx4 v[4:5], v[130:133], off nt
	v_lshl_add_u64 v[4:5], v[2:3], 0, s[40:41]
	s_or_b32 s40, s2, 3
	s_mov_b32 s41, s3
	s_lshl_b64 s[40:41], s[40:41], 10
	s_waitcnt vmcnt(55)
	global_store_dwordx4 v[4:5], v[150:153], off nt
	v_lshl_add_u64 v[4:5], v[2:3], 0, s[40:41]
	s_or_b32 s40, s2, 4
	s_mov_b32 s41, s3
	s_lshl_b64 s[40:41], s[40:41], 10
	s_waitcnt vmcnt(55)
	global_store_dwordx4 v[4:5], v[134:137], off nt
	v_lshl_add_u64 v[4:5], v[2:3], 0, s[40:41]
	s_or_b32 s40, s2, 5
	s_mov_b32 s41, s3
	s_lshl_b64 s[40:41], s[40:41], 10
	s_waitcnt vmcnt(55)
	global_store_dwordx4 v[4:5], v[154:157], off nt
	v_lshl_add_u64 v[4:5], v[2:3], 0, s[40:41]
	s_or_b32 s40, s2, 6
	s_mov_b32 s41, s3
	s_lshl_b64 s[40:41], s[40:41], 10
	s_or_b32 s2, s2, 7
	s_add_i32 s39, s39, 0xb000
	s_waitcnt vmcnt(55)
	global_store_dwordx4 v[4:5], v[138:141], off nt
	v_lshl_add_u64 v[4:5], v[2:3], 0, s[40:41]
	s_lshl_b64 s[40:41], s[2:3], 10
	s_and_b32 s2, s39, 0x18000
	s_add_i32 s2, s31, s2
	s_lshl_b32 s2, s2, 10
	v_lshl_add_u64 v[2:3], v[2:3], 0, s[40:41]
	s_or_b32 s2, s2, s10
	s_waitcnt vmcnt(55)
	global_store_dwordx4 v[4:5], v[158:161], off nt
	s_waitcnt vmcnt(55)
	global_store_dwordx4 v[2:3], v[142:145], off nt
	s_or_b32 s39, s2, 0x400
	buffer_load_dwordx4 v[38:41], v162, s[4:7], s2 offen nt sc1
	buffer_load_dwordx4 v[30:33], v162, s[4:7], s39 offen nt sc1
	s_or_b32 s39, s2, 0x800
	s_or_b32 s40, s2, 0xc00
	buffer_load_dwordx4 v[22:25], v162, s[4:7], s39 offen nt sc1
	buffer_load_dwordx4 v[18:21], v162, s[4:7], s40 offen nt sc1
	s_or_b32 s39, s2, 0x1000
	s_or_b32 s40, s2, 0x1400
	buffer_load_dwordx4 v[14:17], v162, s[4:7], s39 offen nt sc1
	buffer_load_dwordx4 v[10:13], v162, s[4:7], s40 offen nt sc1
	s_or_b32 s39, s2, 0x1800
	s_or_b32 s2, s2, 0x1c00
	buffer_load_dwordx4 v[6:9], v162, s[4:7], s39 offen nt sc1
	buffer_load_dwordx4 v[2:5], v162, s[4:7], s2 offen nt sc1
	v_cvt_pk_f16_f32 v149, v148, v149
	v_cvt_pk_f16_f32 v148, v146, v147
	v_cvt_pk_f16_f32 v133, v132, v133
	v_cvt_pk_f16_f32 v132, v130, v131
	ds_write2_b64 v187, v[148:149], v[132:133] offset0:96 offset1:162
	v_cvt_pk_f16_f32 v131, v152, v153
	v_cvt_pk_f16_f32 v130, v150, v151
	v_cvt_pk_f16_f32 v133, v136, v137
	v_cvt_pk_f16_f32 v132, v134, v135
	ds_write2_b64 v188, v[130:131], v[132:133] offset0:100 offset1:166
	v_cvt_pk_f16_f32 v131, v156, v157
	v_cvt_pk_f16_f32 v130, v154, v155
	v_cvt_pk_f16_f32 v133, v140, v141
	v_cvt_pk_f16_f32 v132, v138, v139
	ds_write2_b64 v189, v[130:131], v[132:133] offset0:104 offset1:170
	v_cvt_pk_f16_f32 v131, v160, v161
	v_cvt_pk_f16_f32 v130, v158, v159
	v_cvt_pk_f16_f32 v133, v144, v145
	v_cvt_pk_f16_f32 v132, v142, v143
	ds_write2_b64 v190, v[130:131], v[132:133] offset0:108 offset1:174
	s_waitcnt lgkmcnt(0)
	s_barrier
	s_barrier
	ds_read_b32 v130, v165
	s_waitcnt lgkmcnt(0)
	v_cmp_gt_i32_e32 vcc, 1, v130
	s_cbranch_vccnz .LBB1_144

.LBB1_148:
	s_mov_b64 s[2:3], s[16:17]
	s_mov_b64 s[8:9], s[20:21]
	s_add_i32 s2, s13, 0x18000
	s_mov_b32 s3, 0
	s_lshl_b64 s[22:23], s[2:3], 10
	v_lshl_add_u64 v[130:131], s[8:9], 0, v[162:163]
	s_add_i32 s2, s13, 0x18001
	v_lshl_add_u64 v[132:133], v[130:131], 0, s[22:23]
	s_lshl_b64 s[8:9], s[2:3], 10
	s_add_i32 s2, s13, 0x18002
	s_waitcnt vmcnt(55)
	global_store_dwordx4 v[132:133], v[126:129], off nt
	s_mov_b64 s[22:23], s[16:17]
	s_mov_b64 s[24:25], s[20:21]
	v_cvt_pk_f16_f32 v129, v128, v129
	v_cvt_pk_f16_f32 v128, v126, v127
	v_lshl_add_u64 v[126:127], v[130:131], 0, s[8:9]
	s_lshl_b64 s[8:9], s[2:3], 10
	s_add_i32 s2, s13, 0x18003
	s_waitcnt vmcnt(55)
	global_store_dwordx4 v[126:127], v[122:125], off nt
	s_nop 1
	v_cvt_pk_f16_f32 v125, v124, v125
	v_cvt_pk_f16_f32 v124, v122, v123
	v_lshl_add_u64 v[122:123], v[130:131], 0, s[8:9]
	s_lshl_b64 s[8:9], s[2:3], 10
	s_add_i32 s2, s13, 0x18004
	s_waitcnt vmcnt(55)
	global_store_dwordx4 v[122:123], v[118:121], off nt
	ds_write2_b64 v1, v[128:129], v[124:125] offset1:66
	s_nop 0
	v_cvt_pk_f16_f32 v121, v120, v121
	v_cvt_pk_f16_f32 v120, v118, v119
	v_lshl_add_u64 v[118:119], v[130:131], 0, s[8:9]
	s_lshl_b64 s[8:9], s[2:3], 10
	s_add_i32 s2, s13, 0x18005
	s_waitcnt vmcnt(55)
	global_store_dwordx4 v[118:119], v[114:117], off nt
	s_nop 1
	v_cvt_pk_f16_f32 v117, v116, v117
	v_cvt_pk_f16_f32 v116, v114, v115
	v_lshl_add_u64 v[114:115], v[130:131], 0, s[8:9]
	s_lshl_b64 s[8:9], s[2:3], 10
	s_add_i32 s2, s13, 0x18006
	s_waitcnt vmcnt(55)
	global_store_dwordx4 v[114:115], v[110:113], off nt
	ds_write2_b64 v1, v[120:121], v[116:117] offset0:132 offset1:198
	s_nop 0
	v_cvt_pk_f16_f32 v113, v112, v113
	v_cvt_pk_f16_f32 v112, v110, v111
	v_lshl_add_u64 v[110:111], v[130:131], 0, s[8:9]
	s_lshl_b64 s[8:9], s[2:3], 10
	s_add_i32 s2, s13, 0x18007
	s_waitcnt vmcnt(55)
	global_store_dwordx4 v[110:111], v[106:109], off nt
	v_add_u32_e32 v110, 0x800, v1
	s_nop 0
	v_cvt_pk_f16_f32 v109, v108, v109
	v_cvt_pk_f16_f32 v108, v106, v107
	v_lshl_add_u64 v[106:107], v[130:131], 0, s[8:9]
	s_lshl_b64 s[8:9], s[2:3], 10
	s_waitcnt vmcnt(55)
	global_store_dwordx4 v[106:107], v[102:105], off nt
	ds_write2_b64 v110, v[112:113], v[108:109] offset0:8 offset1:74
	s_nop 0
	v_cvt_pk_f16_f32 v105, v104, v105
	v_cvt_pk_f16_f32 v104, v102, v103
	v_lshl_add_u64 v[102:103], v[130:131], 0, s[8:9]
	s_add_i32 s8, s98, 0x18040
	s_lshl_b32 s2, s8, 10
	s_waitcnt vmcnt(55)
	global_store_dwordx4 v[102:103], v[94:97], off nt
	s_or_b32 s2, s10, s2
	s_or_b32 s9, s2, 0x400
	v_cvt_pk_f16_f32 v97, v96, v97
	v_cvt_pk_f16_f32 v96, v94, v95
	ds_write2_b64 v110, v[104:105], v[96:97] offset0:140 offset1:206
	buffer_load_dwordx4 v[126:129], v162, s[4:7], s2 offen nt sc1
	buffer_load_dwordx4 v[122:125], v162, s[4:7], s9 offen nt sc1
	s_or_b32 s9, s2, 0x800
	s_or_b32 s11, s2, 0xc00
	buffer_load_dwordx4 v[118:121], v162, s[4:7], s9 offen nt sc1
	buffer_load_dwordx4 v[114:117], v162, s[4:7], s11 offen nt sc1
	s_or_b32 s9, s2, 0x1000
	s_or_b32 s11, s2, 0x1400
	buffer_load_dwordx4 v[110:113], v162, s[4:7], s9 offen nt sc1
	buffer_load_dwordx4 v[106:109], v162, s[4:7], s11 offen nt sc1
	s_or_b32 s9, s2, 0x1800
	s_or_b32 s2, s2, 0x1c00
	buffer_load_dwordx4 v[102:105], v162, s[4:7], s9 offen nt sc1
	buffer_load_dwordx4 v[94:97], v162, s[4:7], s2 offen nt sc1
	s_waitcnt lgkmcnt(0)
	s_barrier
	s_add_i32 s2, s13, 0x18010
	s_lshl_b64 s[22:23], s[2:3], 10
	v_lshl_add_u64 v[130:131], s[24:25], 0, v[162:163]
	s_add_i32 s2, s13, 0x18011
	v_lshl_add_u64 v[132:133], v[130:131], 0, s[22:23]
	s_lshl_b64 s[22:23], s[2:3], 10
	s_add_i32 s2, s13, 0x18012
	s_waitcnt vmcnt(55)
	global_store_dwordx4 v[132:133], v[98:101], off nt
	s_add_i32 s9, s98, 0x18050
	s_mov_b64 s[24:25], s[20:21]
	v_cvt_pk_f16_f32 v101, v100, v101
	v_cvt_pk_f16_f32 v100, v98, v99
	v_lshl_add_u64 v[98:99], v[130:131], 0, s[22:23]
	s_lshl_b64 s[22:23], s[2:3], 10
	s_add_i32 s2, s13, 0x18013
	s_waitcnt vmcnt(55)
	global_store_dwordx4 v[98:99], v[90:93], off nt
	v_add_u32_e32 v98, 0x2000, v1
	s_nop 0
	v_cvt_pk_f16_f32 v93, v92, v93
	v_cvt_pk_f16_f32 v92, v90, v91
	v_lshl_add_u64 v[90:91], v[130:131], 0, s[22:23]
	s_lshl_b64 s[22:23], s[2:3], 10
	s_add_i32 s2, s13, 0x18014
	s_waitcnt vmcnt(55)
	global_store_dwordx4 v[90:91], v[86:89], off nt
	ds_write2_b64 v98, v[100:101], v[92:93] offset0:32 offset1:98
	s_nop 0
	v_cvt_pk_f16_f32 v89, v88, v89
	v_cvt_pk_f16_f32 v88, v86, v87
	v_lshl_add_u64 v[86:87], v[130:131], 0, s[22:23]
	s_lshl_b64 s[22:23], s[2:3], 10
	s_add_i32 s2, s13, 0x18015
	s_waitcnt vmcnt(55)
	global_store_dwordx4 v[86:87], v[82:85], off nt
	s_nop 1
	v_cvt_pk_f16_f32 v85, v84, v85
	v_cvt_pk_f16_f32 v84, v82, v83
	v_lshl_add_u64 v[82:83], v[130:131], 0, s[22:23]
	s_lshl_b64 s[22:23], s[2:3], 10
	s_add_i32 s2, s13, 0x18016
	s_waitcnt vmcnt(55)
	global_store_dwordx4 v[82:83], v[78:81], off nt
	ds_write2_b64 v98, v[88:89], v[84:85] offset0:164 offset1:230
	s_nop 0
	v_cvt_pk_f16_f32 v81, v80, v81
	v_cvt_pk_f16_f32 v80, v78, v79
	v_lshl_add_u64 v[78:79], v[130:131], 0, s[22:23]
	s_lshl_b64 s[22:23], s[2:3], 10
	s_add_i32 s2, s13, 0x18017
	s_waitcnt vmcnt(55)
	global_store_dwordx4 v[78:79], v[74:77], off nt
	v_add_u32_e32 v78, 0x2800, v1
	s_nop 0
	v_cvt_pk_f16_f32 v77, v76, v77
	v_cvt_pk_f16_f32 v76, v74, v75
	v_lshl_add_u64 v[74:75], v[130:131], 0, s[22:23]
	s_lshl_b64 s[22:23], s[2:3], 10
	s_waitcnt vmcnt(55)
	global_store_dwordx4 v[74:75], v[66:69], off nt
	s_lshl_b32 s2, s9, 10
	s_or_b32 s2, s10, s2
	v_cvt_pk_f16_f32 v69, v68, v69
	v_cvt_pk_f16_f32 v68, v66, v67
	v_lshl_add_u64 v[66:67], v[130:131], 0, s[22:23]
	s_waitcnt vmcnt(55)
	global_store_dwordx4 v[66:67], v[58:61], off nt
	ds_write2_b64 v78, v[80:81], v[76:77] offset0:40 offset1:106
	s_or_b32 s11, s2, 0x400
	v_cvt_pk_f16_f32 v61, v60, v61
	v_cvt_pk_f16_f32 v60, v58, v59
	ds_write2_b64 v78, v[68:69], v[60:61] offset0:172 offset1:238
	buffer_load_dwordx4 v[98:101], v162, s[4:7], s2 offen nt sc1
	buffer_load_dwordx4 v[90:93], v162, s[4:7], s11 offen nt sc1
	s_or_b32 s11, s2, 0x800
	s_or_b32 s22, s2, 0xc00
	buffer_load_dwordx4 v[86:89], v162, s[4:7], s11 offen nt sc1
	buffer_load_dwordx4 v[82:85], v162, s[4:7], s22 offen nt sc1
	s_or_b32 s11, s2, 0x1000
	s_or_b32 s22, s2, 0x1400
	buffer_load_dwordx4 v[78:81], v162, s[4:7], s11 offen nt sc1
	buffer_load_dwordx4 v[74:77], v162, s[4:7], s22 offen nt sc1
	s_or_b32 s11, s2, 0x1800
	s_or_b32 s2, s2, 0x1c00
	s_mov_b64 s[22:23], s[16:17]
	buffer_load_dwordx4 v[66:69], v162, s[4:7], s11 offen nt sc1
	buffer_load_dwordx4 v[58:61], v162, s[4:7], s2 offen nt sc1
	s_waitcnt lgkmcnt(0)
	s_barrier
	s_add_i32 s2, s13, 0x18020
	s_lshl_b64 s[22:23], s[2:3], 10
	v_lshl_add_u64 v[130:131], s[24:25], 0, v[162:163]
	s_add_i32 s2, s13, 0x18021
	v_lshl_add_u64 v[132:133], v[130:131], 0, s[22:23]
	s_lshl_b64 s[22:23], s[2:3], 10
	s_waitcnt vmcnt(55)
	global_store_dwordx4 v[132:133], v[70:73], off nt
	s_add_i32 s2, s13, 0x18022
	s_add_i32 s11, s98, 0x18060
	v_cvt_pk_f16_f32 v73, v72, v73
	v_cvt_pk_f16_f32 v72, v70, v71
	v_lshl_add_u64 v[70:71], v[130:131], 0, s[22:23]
	s_waitcnt vmcnt(55)
	global_store_dwordx4 v[70:71], v[62:65], off nt
	s_lshl_b64 s[22:23], s[2:3], 10
	s_add_i32 s2, s13, 0x18023
	v_cvt_pk_f16_f32 v65, v64, v65
	v_cvt_pk_f16_f32 v64, v62, v63
	v_add_u32_e32 v62, 0x4000, v1
	ds_write2_b64 v62, v[72:73], v[64:65] offset0:64 offset1:130
	v_lshl_add_u64 v[62:63], v[130:131], 0, s[22:23]
	s_lshl_b64 s[22:23], s[2:3], 10
	s_waitcnt vmcnt(55)
	global_store_dwordx4 v[62:63], v[54:57], off nt
	s_add_i32 s2, s13, 0x18024
	s_mov_b64 s[24:25], s[20:21]
	v_cvt_pk_f16_f32 v57, v56, v57
	v_cvt_pk_f16_f32 v56, v54, v55
	v_lshl_add_u64 v[54:55], v[130:131], 0, s[22:23]
	s_waitcnt vmcnt(55)
	global_store_dwordx4 v[54:55], v[50:53], off nt
	s_lshl_b64 s[22:23], s[2:3], 10
	s_add_i32 s2, s13, 0x18025
	v_cvt_pk_f16_f32 v53, v52, v53
	v_cvt_pk_f16_f32 v52, v50, v51
	v_add_u32_e32 v50, 0x4400, v1
	ds_write2_b64 v50, v[56:57], v[52:53] offset0:68 offset1:134
	v_lshl_add_u64 v[50:51], v[130:131], 0, s[22:23]
	s_lshl_b64 s[22:23], s[2:3], 10
	s_waitcnt vmcnt(55)
	global_store_dwordx4 v[50:51], v[46:49], off nt
	s_add_i32 s2, s13, 0x18026
	s_add_i32 s98, s98, 0x18070
	v_cvt_pk_f16_f32 v49, v48, v49
	v_cvt_pk_f16_f32 v48, v46, v47
	v_lshl_add_u64 v[46:47], v[130:131], 0, s[22:23]
	s_waitcnt vmcnt(55)
	global_store_dwordx4 v[46:47], v[42:45], off nt
	s_lshl_b64 s[22:23], s[2:3], 10
	s_add_i32 s2, s13, 0x18027
	v_cvt_pk_f16_f32 v45, v44, v45
	v_cvt_pk_f16_f32 v44, v42, v43
	v_add_u32_e32 v42, 0x4800, v1
	ds_write2_b64 v42, v[48:49], v[44:45] offset0:72 offset1:138
	v_lshl_add_u64 v[42:43], v[130:131], 0, s[22:23]
	s_lshl_b64 s[22:23], s[2:3], 10
	s_waitcnt vmcnt(55)
	global_store_dwordx4 v[42:43], v[34:37], off nt
	s_lshl_b32 s2, s11, 10
	s_or_b32 s2, s10, s2
	v_cvt_pk_f16_f32 v37, v36, v37
	v_cvt_pk_f16_f32 v36, v34, v35
	v_lshl_add_u64 v[34:35], v[130:131], 0, s[22:23]
	s_waitcnt vmcnt(55)
	global_store_dwordx4 v[34:35], v[26:29], off nt
	s_or_b32 s22, s2, 0x400
	s_or_b32 s23, s2, 0xc00
	v_cvt_pk_f16_f32 v29, v28, v29
	v_cvt_pk_f16_f32 v28, v26, v27
	v_add_u32_e32 v26, 0x4c00, v1
	ds_write2_b64 v26, v[36:37], v[28:29] offset0:76 offset1:142
	buffer_load_dwordx4 v[70:73], v162, s[4:7], s2 offen nt sc1
	buffer_load_dwordx4 v[62:65], v162, s[4:7], s22 offen nt sc1
	s_or_b32 s22, s2, 0x800
	buffer_load_dwordx4 v[54:57], v162, s[4:7], s22 offen nt sc1
	buffer_load_dwordx4 v[50:53], v162, s[4:7], s23 offen nt sc1
	s_or_b32 s22, s2, 0x1000
	s_or_b32 s23, s2, 0x1400
	buffer_load_dwordx4 v[46:49], v162, s[4:7], s22 offen nt sc1
	buffer_load_dwordx4 v[42:45], v162, s[4:7], s23 offen nt sc1
	s_or_b32 s22, s2, 0x1800
	s_or_b32 s2, s2, 0x1c00
	buffer_load_dwordx4 v[34:37], v162, s[4:7], s22 offen nt sc1
	buffer_load_dwordx4 v[26:29], v162, s[4:7], s2 offen nt sc1
	s_mov_b64 s[22:23], s[16:17]
	s_waitcnt lgkmcnt(0)
	s_barrier
	s_add_i32 s2, s13, 0x18030
	s_lshl_b64 s[22:23], s[2:3], 10
	v_lshl_add_u64 v[130:131], s[24:25], 0, v[162:163]
	s_add_i32 s2, s13, 0x18031
	v_lshl_add_u64 v[132:133], v[130:131], 0, s[22:23]
	s_lshl_b64 s[22:23], s[2:3], 10
	s_waitcnt vmcnt(55)
	global_store_dwordx4 v[132:133], v[38:41], off nt
	s_add_i32 s2, s13, 0x18032
	s_nop 0
	v_cvt_pk_f16_f32 v41, v40, v41
	v_cvt_pk_f16_f32 v40, v38, v39
	v_lshl_add_u64 v[38:39], v[130:131], 0, s[22:23]
	s_waitcnt vmcnt(55)
	global_store_dwordx4 v[38:39], v[30:33], off nt
	s_lshl_b64 s[22:23], s[2:3], 10
	s_add_i32 s2, s13, 0x18033
	v_cvt_pk_f16_f32 v33, v32, v33
	v_cvt_pk_f16_f32 v32, v30, v31
	v_add_u32_e32 v30, 0x6000, v1
	ds_write2_b64 v30, v[40:41], v[32:33] offset0:96 offset1:162
	v_lshl_add_u64 v[30:31], v[130:131], 0, s[22:23]
	s_lshl_b64 s[22:23], s[2:3], 10
	s_waitcnt vmcnt(55)
	global_store_dwordx4 v[30:31], v[22:25], off nt
	s_add_i32 s2, s13, 0x18034
	s_nop 0
	v_cvt_pk_f16_f32 v25, v24, v25
	v_cvt_pk_f16_f32 v24, v22, v23
	v_lshl_add_u64 v[22:23], v[130:131], 0, s[22:23]
	s_waitcnt vmcnt(55)
	global_store_dwordx4 v[22:23], v[18:21], off nt
	s_lshl_b64 s[22:23], s[2:3], 10
	s_add_i32 s2, s13, 0x18035
	v_cvt_pk_f16_f32 v21, v20, v21
	v_cvt_pk_f16_f32 v20, v18, v19
	v_add_u32_e32 v18, 0x6400, v1
	ds_write2_b64 v18, v[24:25], v[20:21] offset0:100 offset1:166
	v_lshl_add_u64 v[18:19], v[130:131], 0, s[22:23]
	s_lshl_b64 s[22:23], s[2:3], 10
	s_waitcnt vmcnt(55)
	global_store_dwordx4 v[18:19], v[14:17], off nt
	s_add_i32 s2, s13, 0x18036
	s_nop 0
	v_cvt_pk_f16_f32 v17, v16, v17
	v_cvt_pk_f16_f32 v16, v14, v15
	v_lshl_add_u64 v[14:15], v[130:131], 0, s[22:23]
	s_waitcnt vmcnt(55)
	global_store_dwordx4 v[14:15], v[10:13], off nt
	s_lshl_b64 s[22:23], s[2:3], 10
	s_add_i32 s2, s13, 0x18037
	v_cvt_pk_f16_f32 v13, v12, v13
	v_cvt_pk_f16_f32 v12, v10, v11
	v_add_u32_e32 v10, 0x6800, v1
	ds_write2_b64 v10, v[16:17], v[12:13] offset0:104 offset1:170
	v_lshl_add_u64 v[10:11], v[130:131], 0, s[22:23]
	s_lshl_b64 s[22:23], s[2:3], 10
	s_waitcnt vmcnt(55)
	global_store_dwordx4 v[10:11], v[6:9], off nt
	s_lshl_b32 s2, s98, 10
	s_or_b32 s2, s10, s2
	v_cvt_pk_f16_f32 v9, v8, v9
	v_cvt_pk_f16_f32 v8, v6, v7
	v_lshl_add_u64 v[6:7], v[130:131], 0, s[22:23]
	s_waitcnt vmcnt(55)
	global_store_dwordx4 v[6:7], v[2:5], off nt
	s_or_b32 s10, s2, 0x400
	s_or_b32 s13, s2, 0xc00
	v_cvt_pk_f16_f32 v5, v4, v5
	v_cvt_pk_f16_f32 v4, v2, v3
	v_add_u32_e32 v2, 0x6c00, v1
	ds_write2_b64 v2, v[8:9], v[4:5] offset0:108 offset1:174
	buffer_load_dwordx4 v[38:41], v162, s[4:7], s2 offen nt sc1
	buffer_load_dwordx4 v[30:33], v162, s[4:7], s10 offen nt sc1
	s_or_b32 s10, s2, 0x800
	buffer_load_dwordx4 v[22:25], v162, s[4:7], s10 offen nt sc1
	buffer_load_dwordx4 v[18:21], v162, s[4:7], s13 offen nt sc1
	s_or_b32 s10, s2, 0x1000
	s_or_b32 s13, s2, 0x1400
	buffer_load_dwordx4 v[14:17], v162, s[4:7], s10 offen nt sc1
	buffer_load_dwordx4 v[10:13], v162, s[4:7], s13 offen nt sc1
	s_or_b32 s10, s2, 0x1800
	s_or_b32 s2, s2, 0x1c00
	buffer_load_dwordx4 v[6:9], v162, s[4:7], s10 offen nt sc1
	buffer_load_dwordx4 v[2:5], v162, s[4:7], s2 offen nt sc1
	s_mov_b64 s[4:5], s[16:17]
	s_mov_b64 s[6:7], s[20:21]
	s_waitcnt lgkmcnt(0)
	s_barrier
	s_or_b32 s2, s12, s8
	s_lshl_b64 s[4:5], s[2:3], 10
	v_lshl_add_u64 v[130:131], s[6:7], 0, v[162:163]
	v_lshl_add_u64 v[132:133], v[130:131], 0, s[4:5]
	s_or_b32 s4, s2, 1
	s_mov_b32 s5, s3
	s_lshl_b64 s[4:5], s[4:5], 10
	s_waitcnt vmcnt(55)
	global_store_dwordx4 v[132:133], v[126:129], off nt
	s_mov_b64 s[6:7], s[20:21]
	s_nop 0
	v_cvt_pk_f16_f32 v129, v128, v129
	v_cvt_pk_f16_f32 v128, v126, v127
	v_lshl_add_u64 v[126:127], v[130:131], 0, s[4:5]
	s_or_b32 s4, s2, 2
	s_mov_b32 s5, s3
	s_waitcnt vmcnt(55)
	global_store_dwordx4 v[126:127], v[122:125], off nt
	s_lshl_b64 s[4:5], s[4:5], 10
	s_nop 0
	v_cvt_pk_f16_f32 v125, v124, v125
	v_cvt_pk_f16_f32 v124, v122, v123
	v_add_u32_e32 v122, 0x8000, v1
	ds_write2_b64 v122, v[128:129], v[124:125] offset0:128 offset1:194
	v_lshl_add_u64 v[122:123], v[130:131], 0, s[4:5]
	s_or_b32 s4, s2, 3
	s_mov_b32 s5, s3
	s_lshl_b64 s[4:5], s[4:5], 10
	s_waitcnt vmcnt(55)
	global_store_dwordx4 v[122:123], v[118:121], off nt
	s_nop 1
	v_cvt_pk_f16_f32 v121, v120, v121
	v_cvt_pk_f16_f32 v120, v118, v119
	v_lshl_add_u64 v[118:119], v[130:131], 0, s[4:5]
	s_or_b32 s4, s2, 4
	s_mov_b32 s5, s3
	s_lshl_b64 s[4:5], s[4:5], 10
	s_waitcnt vmcnt(55)
	global_store_dwordx4 v[118:119], v[114:117], off nt
	v_add_u32_e32 v118, 0x8800, v1
	s_nop 0
	v_cvt_pk_f16_f32 v117, v116, v117
	v_cvt_pk_f16_f32 v116, v114, v115
	v_lshl_add_u64 v[114:115], v[130:131], 0, s[4:5]
	s_or_b32 s4, s2, 5
	s_mov_b32 s5, s3
	s_lshl_b64 s[4:5], s[4:5], 10
	s_waitcnt vmcnt(55)
	global_store_dwordx4 v[114:115], v[110:113], off nt
	ds_write2_b64 v118, v[120:121], v[116:117] offset0:4 offset1:70
	s_nop 0
	v_cvt_pk_f16_f32 v113, v112, v113
	v_cvt_pk_f16_f32 v112, v110, v111
	v_lshl_add_u64 v[110:111], v[130:131], 0, s[4:5]
	s_or_b32 s4, s2, 6
	s_mov_b32 s5, s3
	s_lshl_b64 s[4:5], s[4:5], 10
	s_or_b32 s2, s2, 7
	s_waitcnt vmcnt(55)
	global_store_dwordx4 v[110:111], v[106:109], off nt
	s_nop 1
	v_cvt_pk_f16_f32 v109, v108, v109
	v_cvt_pk_f16_f32 v108, v106, v107
	v_lshl_add_u64 v[106:107], v[130:131], 0, s[4:5]
	s_lshl_b64 s[4:5], s[2:3], 10
	s_waitcnt vmcnt(55)
	global_store_dwordx4 v[106:107], v[102:105], off nt
	ds_write2_b64 v118, v[112:113], v[108:109] offset0:136 offset1:202
	s_or_b32 s2, s12, s9
	v_cvt_pk_f16_f32 v105, v104, v105
	v_cvt_pk_f16_f32 v104, v102, v103
	v_lshl_add_u64 v[102:103], v[130:131], 0, s[4:5]
	s_waitcnt vmcnt(55)
	global_store_dwordx4 v[102:103], v[94:97], off nt
	s_mov_b64 s[4:5], s[16:17]
	s_nop 0
	v_cvt_pk_f16_f32 v97, v96, v97
	v_cvt_pk_f16_f32 v96, v94, v95
	v_add_u32_e32 v94, 0x9000, v1
	ds_write2_b64 v94, v[104:105], v[96:97] offset0:12 offset1:78
	s_waitcnt lgkmcnt(0)
	s_barrier
	s_lshl_b64 s[4:5], s[2:3], 10
	v_lshl_add_u64 v[94:95], s[6:7], 0, v[162:163]
	v_lshl_add_u64 v[96:97], v[94:95], 0, s[4:5]
	s_or_b32 s4, s2, 1
	s_mov_b32 s5, s3
	s_lshl_b64 s[4:5], s[4:5], 10
	s_waitcnt vmcnt(47)
	global_store_dwordx4 v[96:97], v[98:101], off nt
	v_cvt_pk_f16_f32 v96, v98, v99
	v_cvt_pk_f16_f32 v97, v100, v101
	v_lshl_add_u64 v[98:99], v[94:95], 0, s[4:5]
	s_or_b32 s4, s2, 2
	s_mov_b32 s5, s3
	s_waitcnt vmcnt(47)
	global_store_dwordx4 v[98:99], v[90:93], off nt
	s_lshl_b64 s[4:5], s[4:5], 10
	s_mov_b64 s[6:7], s[20:21]
	v_cvt_pk_f16_f32 v93, v92, v93
	v_cvt_pk_f16_f32 v92, v90, v91
	v_add_u32_e32 v90, 0xa000, v1
	ds_write2_b64 v90, v[96:97], v[92:93] offset0:160 offset1:226
	v_lshl_add_u64 v[90:91], v[94:95], 0, s[4:5]
	s_or_b32 s4, s2, 3
	s_mov_b32 s5, s3
	s_lshl_b64 s[4:5], s[4:5], 10
	s_waitcnt vmcnt(47)
	global_store_dwordx4 v[90:91], v[86:89], off nt
	s_nop 1
	v_cvt_pk_f16_f32 v89, v88, v89
	v_cvt_pk_f16_f32 v88, v86, v87
	v_lshl_add_u64 v[86:87], v[94:95], 0, s[4:5]
	s_or_b32 s4, s2, 4
	s_mov_b32 s5, s3
	s_lshl_b64 s[4:5], s[4:5], 10
	s_waitcnt vmcnt(47)
	global_store_dwordx4 v[86:87], v[82:85], off nt
	v_add_u32_e32 v86, 0xa800, v1
	s_nop 0
	v_cvt_pk_f16_f32 v85, v84, v85
	v_cvt_pk_f16_f32 v84, v82, v83
	v_lshl_add_u64 v[82:83], v[94:95], 0, s[4:5]
	s_or_b32 s4, s2, 5
	s_mov_b32 s5, s3
	s_lshl_b64 s[4:5], s[4:5], 10
	s_waitcnt vmcnt(47)
	global_store_dwordx4 v[82:83], v[78:81], off nt
	ds_write2_b64 v86, v[88:89], v[84:85] offset0:36 offset1:102
	s_nop 0
	v_cvt_pk_f16_f32 v81, v80, v81
	v_cvt_pk_f16_f32 v80, v78, v79
	v_lshl_add_u64 v[78:79], v[94:95], 0, s[4:5]
	s_or_b32 s4, s2, 6
	s_mov_b32 s5, s3
	s_lshl_b64 s[4:5], s[4:5], 10
	s_or_b32 s2, s2, 7
	s_waitcnt vmcnt(47)
	global_store_dwordx4 v[78:79], v[74:77], off nt
	s_nop 1
	v_cvt_pk_f16_f32 v77, v76, v77
	v_cvt_pk_f16_f32 v76, v74, v75
	v_lshl_add_u64 v[74:75], v[94:95], 0, s[4:5]
	s_lshl_b64 s[4:5], s[2:3], 10
	s_waitcnt vmcnt(47)
	global_store_dwordx4 v[74:75], v[66:69], off nt
	ds_write2_b64 v86, v[80:81], v[76:77] offset0:168 offset1:234
	s_or_b32 s2, s12, s11
	v_cvt_pk_f16_f32 v69, v68, v69
	v_cvt_pk_f16_f32 v68, v66, v67
	v_lshl_add_u64 v[66:67], v[94:95], 0, s[4:5]
	s_waitcnt vmcnt(47)
	global_store_dwordx4 v[66:67], v[58:61], off nt
	s_mov_b64 s[4:5], s[16:17]
	s_nop 0
	v_cvt_pk_f16_f32 v61, v60, v61
	v_cvt_pk_f16_f32 v60, v58, v59
	v_add_u32_e32 v58, 0xb000, v1
	ds_write2_b64 v58, v[68:69], v[60:61] offset0:44 offset1:110
	s_waitcnt lgkmcnt(0)
	s_barrier
	s_lshl_b64 s[4:5], s[2:3], 10
	v_lshl_add_u64 v[58:59], s[6:7], 0, v[162:163]
	v_lshl_add_u64 v[60:61], v[58:59], 0, s[4:5]
	s_or_b32 s4, s2, 1
	s_mov_b32 s5, s3
	s_lshl_b64 s[4:5], s[4:5], 10
	v_lshl_add_u64 v[66:67], v[58:59], 0, s[4:5]
	s_or_b32 s4, s2, 2
	s_mov_b32 s5, s3
	s_waitcnt vmcnt(39)
	global_store_dwordx4 v[60:61], v[70:73], off nt
	v_cvt_pk_f16_f32 v61, v72, v73
	v_cvt_pk_f16_f32 v60, v70, v71
	s_waitcnt vmcnt(39)
	global_store_dwordx4 v[66:67], v[62:65], off nt
	s_lshl_b64 s[4:5], s[4:5], 10
	s_nop 0
	v_cvt_pk_f16_f32 v65, v64, v65
	v_cvt_pk_f16_f32 v64, v62, v63
	v_add_u32_e32 v62, 0xc400, v1
	ds_write2_b64 v62, v[60:61], v[64:65] offset0:64 offset1:130
	v_lshl_add_u64 v[60:61], v[58:59], 0, s[4:5]
	s_or_b32 s4, s2, 3
	s_mov_b32 s5, s3
	s_lshl_b64 s[4:5], s[4:5], 10
	s_waitcnt vmcnt(39)
	global_store_dwordx4 v[60:61], v[54:57], off nt
	s_nop 1
	v_cvt_pk_f16_f32 v57, v56, v57
	v_cvt_pk_f16_f32 v56, v54, v55
	v_lshl_add_u64 v[54:55], v[58:59], 0, s[4:5]
	s_or_b32 s4, s2, 4
	s_mov_b32 s5, s3
	s_waitcnt vmcnt(39)
	global_store_dwordx4 v[54:55], v[50:53], off nt
	s_lshl_b64 s[4:5], s[4:5], 10
	s_nop 0
	v_cvt_pk_f16_f32 v53, v52, v53
	v_cvt_pk_f16_f32 v52, v50, v51
	v_add_u32_e32 v50, 0xc800, v1
	ds_write2_b64 v50, v[56:57], v[52:53] offset0:68 offset1:134
	v_lshl_add_u64 v[50:51], v[58:59], 0, s[4:5]
	s_or_b32 s4, s2, 5
	s_mov_b32 s5, s3
	s_lshl_b64 s[4:5], s[4:5], 10
	s_waitcnt vmcnt(39)
	global_store_dwordx4 v[50:51], v[46:49], off nt
	s_nop 1
	v_cvt_pk_f16_f32 v49, v48, v49
	v_cvt_pk_f16_f32 v48, v46, v47
	v_lshl_add_u64 v[46:47], v[58:59], 0, s[4:5]
	s_or_b32 s4, s2, 6
	s_mov_b32 s5, s3
	s_waitcnt vmcnt(39)
	global_store_dwordx4 v[46:47], v[42:45], off nt
	s_lshl_b64 s[4:5], s[4:5], 10
	s_or_b32 s2, s2, 7
	v_cvt_pk_f16_f32 v45, v44, v45
	v_cvt_pk_f16_f32 v44, v42, v43
	v_add_u32_e32 v42, 0xcc00, v1
	ds_write2_b64 v42, v[48:49], v[44:45] offset0:72 offset1:138
	v_lshl_add_u64 v[42:43], v[58:59], 0, s[4:5]
	s_lshl_b64 s[4:5], s[2:3], 10
	s_waitcnt vmcnt(39)
	global_store_dwordx4 v[42:43], v[34:37], off nt
	s_or_b32 s2, s12, s98
	s_nop 0
	v_cvt_pk_f16_f32 v37, v36, v37
	v_cvt_pk_f16_f32 v36, v34, v35
	v_lshl_add_u64 v[34:35], v[58:59], 0, s[4:5]
	s_waitcnt vmcnt(39)
	global_store_dwordx4 v[34:35], v[26:29], off nt
	s_mov_b64 s[4:5], s[16:17]
	s_nop 0
	v_cvt_pk_f16_f32 v29, v28, v29
	v_cvt_pk_f16_f32 v28, v26, v27
	v_add_u32_e32 v26, 0xd000, v1
	ds_write2_b64 v26, v[36:37], v[28:29] offset0:76 offset1:142
	s_waitcnt lgkmcnt(0)
	s_barrier
	s_lshl_b64 s[4:5], s[2:3], 10
	v_lshl_add_u64 v[26:27], s[20:21], 0, v[162:163]
	v_lshl_add_u64 v[28:29], v[26:27], 0, s[4:5]
	s_or_b32 s4, s2, 1
	s_mov_b32 s5, s3
	s_lshl_b64 s[4:5], s[4:5], 10
	v_lshl_add_u64 v[34:35], v[26:27], 0, s[4:5]
	s_or_b32 s4, s2, 2
	s_mov_b32 s5, s3
	s_waitcnt vmcnt(31)
	global_store_dwordx4 v[28:29], v[38:41], off nt
	v_cvt_pk_f16_f32 v29, v40, v41
	v_cvt_pk_f16_f32 v28, v38, v39
	s_waitcnt vmcnt(31)
	global_store_dwordx4 v[34:35], v[30:33], off nt
	s_lshl_b64 s[4:5], s[4:5], 10
	s_nop 0
	v_cvt_pk_f16_f32 v33, v32, v33
	v_cvt_pk_f16_f32 v32, v30, v31
	v_add_u32_e32 v30, 0xe400, v1
	ds_write2_b64 v30, v[28:29], v[32:33] offset0:96 offset1:162
	v_lshl_add_u64 v[28:29], v[26:27], 0, s[4:5]
	s_or_b32 s4, s2, 3
	s_mov_b32 s5, s3
	s_lshl_b64 s[4:5], s[4:5], 10
	s_waitcnt vmcnt(31)
	global_store_dwordx4 v[28:29], v[22:25], off nt
	s_nop 1
	v_cvt_pk_f16_f32 v25, v24, v25
	v_cvt_pk_f16_f32 v24, v22, v23
	v_lshl_add_u64 v[22:23], v[26:27], 0, s[4:5]
	s_or_b32 s4, s2, 4
	s_mov_b32 s5, s3
	s_waitcnt vmcnt(31)
	global_store_dwordx4 v[22:23], v[18:21], off nt
	s_lshl_b64 s[4:5], s[4:5], 10
	s_nop 0
	v_cvt_pk_f16_f32 v21, v20, v21
	v_cvt_pk_f16_f32 v20, v18, v19
	v_add_u32_e32 v18, 0xe800, v1
	ds_write2_b64 v18, v[24:25], v[20:21] offset0:100 offset1:166
	v_lshl_add_u64 v[18:19], v[26:27], 0, s[4:5]
	s_or_b32 s4, s2, 5
	s_mov_b32 s5, s3
	s_lshl_b64 s[4:5], s[4:5], 10
	s_waitcnt vmcnt(31)
	global_store_dwordx4 v[18:19], v[14:17], off nt
	s_nop 1
	v_cvt_pk_f16_f32 v17, v16, v17
	v_cvt_pk_f16_f32 v16, v14, v15
	v_lshl_add_u64 v[14:15], v[26:27], 0, s[4:5]
	s_or_b32 s4, s2, 6
	s_mov_b32 s5, s3
	s_waitcnt vmcnt(31)
	global_store_dwordx4 v[14:15], v[10:13], off nt
	s_lshl_b64 s[4:5], s[4:5], 10
	s_or_b32 s2, s2, 7
	v_cvt_pk_f16_f32 v13, v12, v13
	v_cvt_pk_f16_f32 v12, v10, v11
	v_add_u32_e32 v10, 0xec00, v1
	ds_write2_b64 v10, v[16:17], v[12:13] offset0:104 offset1:170
	v_lshl_add_u64 v[10:11], v[26:27], 0, s[4:5]
	s_lshl_b64 s[2:3], s[2:3], 10
	s_waitcnt vmcnt(31)
	global_store_dwordx4 v[10:11], v[6:9], off nt
	v_add_u32_e32 v1, 0xf000, v1
	s_nop 0
	v_cvt_pk_f16_f32 v9, v8, v9
	v_cvt_pk_f16_f32 v8, v6, v7
	v_lshl_add_u64 v[6:7], v[26:27], 0, s[2:3]
	s_waitcnt vmcnt(31)
	global_store_dwordx4 v[6:7], v[2:5], off nt
	s_nop 1
	v_cvt_pk_f16_f32 v5, v4, v5
	v_cvt_pk_f16_f32 v4, v2, v3
	ds_write2_b64 v1, v[8:9], v[4:5] offset0:108 offset1:174
	v_mov_b32_e32 v1, 0x22634
	s_waitcnt lgkmcnt(0)
	s_barrier
	s_barrier
	ds_read_b32 v2, v1
	s_waitcnt lgkmcnt(0)
	v_cmp_gt_i32_e32 vcc, 1, v2
	s_cbranch_vccnz .LBB1_151
